# v26: v25 + forgetting-attention bias-fill decay words prefetched into L2 before the fill loop
# baseline (speedup 1.0000x reference)
; __device__ __forceinline__ void fox_fill_bias(const Frame& F, const Args& A, char* lds, int h, int klo, int khi) {
;     int tid = threadIdx.x; asm volatile("" : "+v"(tid));
;     const float* FLOC = (const float*)(A.ws + WS_FLOC);
;     const float* inclL = (const float*)(lds + T_INCL); float* biasL = (float*)(lds + fox::ATT_BIAS_OFF);
;     for (int s = klo + tid; s < khi; s += 512) { const int c = s >> 6; const float off = c ? inclL[h * 128 + c - 1] : 0.f;
;         biasL[s] = -(off + FLOC[h * S_ + s]) * 11.313708498984761f; }
.LBB0_701:
	v_mov_b32_e32 v5, v0
	v_lshlrev_b32_e32 v3, 6, v3
	s_nop 0
	v_lshl_add_u32 v4, v2, 6, v5
	v_cmp_lt_i32_e32 vcc, v4, v3
	s_and_saveexec_b64 s[6:7], vcc
	s_cbranch_execz .LBB0_706
	v_lshlrev_b32_e32 v2, 8, v2
	s_lshl_b32 s1, s10, 9
	v_add_u32_e32 v2, 0, v2
	s_add_i32 s1, s1, 0
	v_add_u32_e32 v2, 0x11000, v2
	s_add_i32 s1, s1, 0x19400
	s_lshl_b32 s26, s10, 13
	v_lshl_add_u32 v2, v5, 2, v2
	s_mov_b64 s[22:23], 0
	v_add_u32_e32 v9, s26, v4
	v_lshlrev_b32_e32 v9, 2, v9
	global_load_dword v8, v9, s[14:15]
	global_load_dword v8, v9, s[14:15] offset:2048
	v_add_u32_e32 v9, 0x1000, v9
	global_load_dword v8, v9, s[14:15]
	global_load_dword v8, v9, s[14:15] offset:2048
	v_add_u32_e32 v9, 0x1000, v9
	global_load_dword v8, v9, s[14:15]
	global_load_dword v8, v9, s[14:15] offset:2048
	v_add_u32_e32 v9, 0x1000, v9
	global_load_dword v8, v9, s[14:15]
	global_load_dword v8, v9, s[14:15] offset:2048
	s_branch .LBB0_704
